# speedup vs baseline: 1.1809x; 1.0069x over previous
.Lco_noin1:
	s_lshl_b32 s11, s75, 6
	v_add_u32_e32 v69, s11, v73
	s_and_b32 s12, s10, 3
	s_lshl_b32 s12, s12, 4
	v_lshrrev_b32_e32 v0, 2, v73
	v_add_u32_e32 v0, s12, v0
	v_and_b32_e32 v1, 3, v73
	v_mul_u32_u24_e32 v49, 0x50, v0
	v_lshl_add_u32 v49, v1, 4, v49
	v_add_u32_e32 v0, s11, v0
	v_lshlrev_b32_e32 v1, 2, v1
	v_add_u32_e32 v1, s3, v1
	v_lshl_add_u32 v0, v0, 9, v1
	v_lshlrev_b32_e32 v0, 2, v0
	s_cmp_gt_u32 s10, 3
	s_cselect_b64 s[16:17], s[62:63], s[46:47]
	s_cselect_b64 s[18:19], s[52:53], s[62:63]
	s_cselect_b64 s[20:21], s[54:55], s[62:63]
	s_cselect_b32 s13, 0x200000, 0
	s_cselect_b32 s14, 0, 0x100000
	s_cselect_b32 s15, 0x3c00, 0
	v_add_u32_e32 v1, s13, v0
	v_add_u32_e32 v2, s14, v0
	v_add_u32_e32 v49, s15, v49
	v_lshlrev_b32_e32 v3, 2, v69
	global_load_dwordx4 v[36:39], v1, s[16:17]
	global_load_dwordx4 v[40:43], v0, s[18:19]
	global_load_dwordx4 v[44:47], v2, s[20:21]
	global_load_dword v48, v3, s[60:61]
	v_cmp_gt_u32_e32 vcc, 4, v98
	s_and_saveexec_b64 s[14:15], vcc
	v_mov_b32_e32 v4, 0x26c10
	v_lshl_add_u32 v4, v98, 2, v4
	ds_write_b32 v4, v34
	s_mov_b64 exec, s[14:15]
	v_cmp_eq_u32_e32 vcc, 0, v98
	s_and_saveexec_b64 s[14:15], vcc
	v_mov_b32_e32 v4, 0x26c00
	ds_write2_b32 v4, v34, v34 offset1:1
	s_mov_b64 exec, s[14:15]
	v_mov_b32_e32 v159, 0
	v_mov_b32_e32 v9, 0
	v_mov_b32_e32 v18, 0
	v_mov_b32_e32 v129, 0
	v_mov_b32_e32 v130, 0
	v_mov_b32_e32 v71, 0
	v_mov_b32_e32 v158, 0
	v_mov_b32_e32 v131, 0
	v_mov_b32_e32 v19, 0
	v_mov_b32_e32 v132, 0
	v_mov_b32_e32 v133, 0
	v_mov_b32_e32 v81, 0
	v_mov_b32_e32 v157, 0
	v_mov_b32_e32 v134, 0
	v_mov_b32_e32 v20, 0
	v_mov_b32_e32 v135, 0
	v_mov_b32_e32 v136, 0
	v_mov_b32_e32 v85, 0
	v_mov_b32_e32 v156, 0
	v_mov_b32_e32 v137, 0
	v_mov_b32_e32 v21, 0
	v_mov_b32_e32 v138, 0
	v_mov_b32_e32 v139, 0
	v_mov_b32_e32 v86, 0
	v_mov_b32_e32 v155, 0
	v_mov_b32_e32 v140, 0
	v_mov_b32_e32 v22, 0
	v_mov_b32_e32 v141, 0
	v_mov_b32_e32 v142, 0
	v_mov_b32_e32 v87, 0
	v_mov_b32_e32 v154, 0
	v_mov_b32_e32 v143, 0
	v_mov_b32_e32 v23, 0
	v_mov_b32_e32 v144, 0
	v_mov_b32_e32 v145, 0
	v_mov_b32_e32 v88, 0
	v_mov_b32_e32 v153, 0
	v_mov_b32_e32 v146, 0
	v_mov_b32_e32 v24, 0
	v_mov_b32_e32 v147, 0
	v_mov_b32_e32 v148, 0
	v_mov_b32_e32 v89, 0
	v_mov_b32_e32 v149, 0
	v_mov_b32_e32 v150, 0
	v_mov_b32_e32 v25, 0
	v_mov_b32_e32 v151, 0
	v_mov_b32_e32 v152, 0
	v_mov_b32_e32 v90, 0
	v_mov_b32_e32 v128, 0
	v_mov_b32_e32 v121, 0
	v_mov_b32_e32 v26, 0
	v_mov_b32_e32 v123, 0
	v_mov_b32_e32 v125, 0
	v_mov_b32_e32 v91, 0
	v_mov_b32_e32 v127, 0
	v_mov_b32_e32 v122, 0
	v_mov_b32_e32 v27, 0
	v_mov_b32_e32 v124, 0
	v_mov_b32_e32 v126, 0
	v_mov_b32_e32 v92, 0
	v_mov_b32_e32 v120, 0
	v_mov_b32_e32 v112, 0
	v_mov_b32_e32 v28, 0
	v_mov_b32_e32 v115, 0
	v_mov_b32_e32 v117, 0
	v_mov_b32_e32 v93, 0
	v_mov_b32_e32 v119, 0
	v_mov_b32_e32 v113, 0
	v_mov_b32_e32 v29, 0
	v_mov_b32_e32 v116, 0
	v_mov_b32_e32 v118, 0
	v_mov_b32_e32 v94, 0
	v_mov_b32_e32 v114, 0
	v_mov_b32_e32 v100, 0
	v_mov_b32_e32 v30, 0
	v_mov_b32_e32 v103, 0
	v_mov_b32_e32 v107, 0
	v_mov_b32_e32 v95, 0
	v_mov_b32_e32 v111, 0
	v_mov_b32_e32 v101, 0
	v_mov_b32_e32 v31, 0
	v_mov_b32_e32 v104, 0
	v_mov_b32_e32 v108, 0
	v_mov_b32_e32 v96, 0
	v_mov_b32_e32 v17, 0
	v_mov_b32_e32 v102, 0
	v_mov_b32_e32 v32, 0
	v_mov_b32_e32 v105, 0
	v_mov_b32_e32 v109, 0
	v_mov_b32_e32 v97, 0
	v_mov_b32_e32 v8, 0
	v_mov_b32_e32 v16, 0
	v_mov_b32_e32 v33, 0
	v_mov_b32_e32 v106, 0
	v_mov_b32_e32 v110, 0
	v_mov_b32_e32 v99, 0
	s_waitcnt vmcnt(0)
	ds_write_b128 v49, v[36:39]
	ds_write_b128 v49, v[40:43] offset:5120
	ds_write_b128 v49, v[44:47] offset:10240
	v_mul_u32_u24_e32 v0, 0x50, v73
	s_lshl_b32 s12, s10, 3
	v_add_u32_e32 v0, s12, v0
	s_lshl_b32 s12, s10, 1
	s_add_i32 s13, s3, s12
	s_waitcnt lgkmcnt(0)
	s_barrier
	ds_read_b64 v[36:37], v0
	ds_read_b64 v[38:39], v0 offset:5120
	ds_read_b64 v[40:41], v0 offset:10240
	ds_read_b64 v[42:43], v0 offset:15360
	ds_read_b64 v[44:45], v0 offset:20480
	ds_read_b64 v[46:47], v0 offset:25600
	s_movk_i32 s84, 0x1000
	s_mov_b64 s[34:35], 0
	s_waitcnt lgkmcnt(0)
	v_mul_f32_e64 v50, v48, |v36|
	v_cmp_neq_f32_e64 s[16:17], 0, v38
	v_cmp_neq_f32_e64 s[18:19], 0, v40
	v_cmp_neq_f32_e64 s[20:21], 0, v42
	v_cmp_neq_f32_e64 s[22:23], 0, v50
	v_cndmask_b32_e64 v51, v42, v40, s[18:19]
	v_cndmask_b32_e64 v52, 2, 1, s[18:19]
	v_cndmask_b32_e64 v51, v51, v38, s[16:17]
	v_cndmask_b32_e64 v52, v52, 0, s[16:17]
	s_or_b64 s[24:25], s[16:17], s[18:19]
	s_and_b64 s[28:29], s[16:17], s[18:19]
	s_and_b64 s[30:31], s[24:25], s[20:21]
	s_or_b64 s[24:25], s[24:25], s[20:21]
	s_or_b64 s[28:29], s[28:29], s[30:31]
	s_and_b64 s[26:27], s[22:23], s[24:25]
	s_and_b64 s[28:29], s[28:29], s[22:23]
	s_bcnt1_i32_b64 s85, s[26:27]
	s_cmp_lg_u64 s[28:29], 0
	s_cselect_b32 s36, 0x8000, 0
	s_or_b32 s36, s36, 0x5c3a0000
	s_or_b32 s85, s85, s36
	s_add_i32 s36, s13, 0
	s_lshl_b32 s36, s36, 3
	s_add_i32 s87, s36, s75
	s_lshl_b32 s37, s87, 11
	s_add_i32 s37, s37, 0x800000
	s_lshl_b32 s87, s87, 7
	s_add_i32 s87, s87, 0x600000
	s_and_saveexec_b64 s[38:39], s[4:5]
	s_cbranch_execz .Lco_nocnt0
	v_mov_b32_e32 v53, s87
	v_mov_b32_e32 v54, s85
	global_store_dword v53, v54, s[66:67] sc1
.Lco_nocnt0:
	s_mov_b64 exec, s[38:39]
	v_lshlrev_b32_e64 v53, v52, s84
	v_lshlrev_b32_e32 v54, 3, v69
	v_sub_u32_e32 v54, v54, v53
	v_and_b32_e32 v56, 0xffff, v54
	v_mul_f32_e32 v57, v50, v51
	v_mul_f32_e32 v58, v44, v51
	v_mul_f32_e32 v59, v46, v51
	v_and_b32_e32 v55, 0x7fffffff, v50
	v_div_scale_f32 v61, s[30:31], v55, v55, 2.0
	v_rcp_f32_e32 v62, v61
	v_div_scale_f32 v55, vcc, 2.0, v55, 2.0
	v_fma_f32 v53, -v61, v62, 1.0
	v_fmac_f32_e32 v62, v53, v62
	v_mul_f32_e32 v53, v55, v62
	v_fma_f32 v54, -v61, v53, v55
	v_fmac_f32_e32 v53, v54, v62
	v_fma_f32 v55, -v61, v53, v55
	v_div_fmas_f32 v55, v55, v62, v53
	v_div_fixup_f32 v60, v55, |v50|, 2.0
	v_or_b32_e32 v56, 0x5c3a0000, v56
	v_mov_b32_e32 v61, 0x5c3a
	v_mbcnt_lo_u32_b32 v53, s26, 0
	v_mbcnt_hi_u32_b32 v53, s27, v53
	v_lshl_add_u32 v4, v53, 5, s37
	s_and_saveexec_b64 s[38:39], s[26:27]
	s_cbranch_execz .Lco_nost0
	global_store_dwordx4 v4, v[56:59], s[66:67] sc1
	global_store_dwordx2 v4, v[60:61], s[66:67] offset:16 sc1
.Lco_nost0:
	s_mov_b64 exec, s[38:39]
	v_mul_f32_e64 v50, v48, |v37|
	v_cmp_neq_f32_e64 s[16:17], 0, v39
	v_cmp_neq_f32_e64 s[18:19], 0, v41
	v_cmp_neq_f32_e64 s[20:21], 0, v43
	v_cmp_neq_f32_e64 s[22:23], 0, v50
	v_cndmask_b32_e64 v51, v43, v41, s[18:19]
	v_cndmask_b32_e64 v52, 2, 1, s[18:19]
	v_cndmask_b32_e64 v51, v51, v39, s[16:17]
	v_cndmask_b32_e64 v52, v52, 0, s[16:17]
	s_or_b64 s[24:25], s[16:17], s[18:19]
	s_and_b64 s[28:29], s[16:17], s[18:19]
	s_and_b64 s[30:31], s[24:25], s[20:21]
	s_or_b64 s[24:25], s[24:25], s[20:21]
	s_or_b64 s[28:29], s[28:29], s[30:31]
	s_and_b64 s[26:27], s[22:23], s[24:25]
	s_and_b64 s[28:29], s[28:29], s[22:23]
	s_bcnt1_i32_b64 s86, s[26:27]
	s_cmp_lg_u64 s[28:29], 0
	s_cselect_b32 s36, 0x8000, 0
	s_or_b32 s36, s36, 0x5c3a0000
	s_or_b32 s86, s86, s36
	s_add_i32 s36, s13, 1
	s_lshl_b32 s36, s36, 3
	s_add_i32 s88, s36, s75
	s_lshl_b32 s37, s88, 11
	s_add_i32 s37, s37, 0x800000
	s_lshl_b32 s88, s88, 7
	s_add_i32 s88, s88, 0x600000
	s_and_saveexec_b64 s[38:39], s[4:5]
	s_cbranch_execz .Lco_nocnt1
	v_mov_b32_e32 v53, s88
	v_mov_b32_e32 v54, s86
	global_store_dword v53, v54, s[66:67] sc1
.Lco_nocnt1:
	s_mov_b64 exec, s[38:39]
	v_lshlrev_b32_e64 v53, v52, s84
	v_lshlrev_b32_e32 v54, 3, v69
	v_sub_u32_e32 v54, v54, v53
	v_and_b32_e32 v76, 0xffff, v54
	v_mul_f32_e32 v77, v50, v51
	v_mul_f32_e32 v78, v45, v51
	v_mul_f32_e32 v79, v47, v51
	v_and_b32_e32 v55, 0x7fffffff, v50
	v_div_scale_f32 v61, s[30:31], v55, v55, 2.0
	v_rcp_f32_e32 v62, v61
	v_div_scale_f32 v55, vcc, 2.0, v55, 2.0
	v_fma_f32 v53, -v61, v62, 1.0
	v_fmac_f32_e32 v62, v53, v62
	v_mul_f32_e32 v53, v55, v62
	v_fma_f32 v54, -v61, v53, v55
	v_fmac_f32_e32 v53, v54, v62
	v_fma_f32 v55, -v61, v53, v55
	v_div_fmas_f32 v55, v55, v62, v53
	v_div_fixup_f32 v82, v55, |v50|, 2.0
	v_or_b32_e32 v76, 0x5c3a0000, v76
	v_mov_b32_e32 v83, 0x5c3a
	v_mbcnt_lo_u32_b32 v53, s26, 0
	v_mbcnt_hi_u32_b32 v53, s27, v53
	v_lshl_add_u32 v5, v53, 5, s37
	s_and_saveexec_b64 s[38:39], s[26:27]
	s_cbranch_execz .Lco_nost1
	global_store_dwordx4 v5, v[76:79], s[66:67] sc1
	global_store_dwordx2 v5, v[82:83], s[66:67] offset:16 sc1

.Lco_noin2:
	s_cmp_gt_u32 s10, 1
	s_cbranch_scc1 .Lco_nopoll
	s_lshl_b32 s36, s33, 7
	v_add_u32_e32 v0, s36, v98
	v_lshlrev_b32_e32 v0, 7, v0
	v_add_u32_e32 v0, 0x600000, v0
	s_mov_b32 s37, 0

.Lco_nopoll:
	s_waitcnt lgkmcnt(0)
	s_barrier
	v_mov_b32_e32 v76, 0
	v_mov_b32_e32 v77, 0
	v_mov_b32_e32 v78, 0
	v_mov_b32_e32 v79, 0
	ds_write_b128 v74, v[76:79]
	ds_write_b128 v74, v[76:79] offset:8192
	ds_write_b128 v74, v[76:79] offset:16384
	ds_write_b128 v74, v[76:79] offset:24576
	ds_write_b128 v74, v[76:79] offset:32768
	ds_write_b128 v74, v[76:79] offset:40960
	ds_write_b128 v74, v[76:79] offset:49152
	ds_write_b128 v74, v[76:79] offset:57344
	v_mov_b32_e32 v0, 0x26400
	v_lshl_add_u32 v0, v75, 5, v0
	ds_read_b128 v[36:39], v0
	ds_read_b128 v[40:43], v0 offset:16
	s_waitcnt lgkmcnt(0)
	v_or3_b32 v44, v36, v37, v38
	v_or3_b32 v44, v44, v39, v40
	v_or3_b32 v44, v44, v41, v42
	v_or_b32_e32 v44, v44, v43
	v_bfe_u32 v44, v44, 15, 1
	v_and_b32_e32 v36, 0x7f, v36
	v_and_b32_e32 v37, 0x7f, v37
	v_and_b32_e32 v38, 0x7f, v38
	v_and_b32_e32 v39, 0x7f, v39
	v_and_b32_e32 v40, 0x7f, v40
	v_and_b32_e32 v41, 0x7f, v41
	v_and_b32_e32 v42, 0x7f, v42
	v_and_b32_e32 v43, 0x7f, v43
	v_mov_b32_e32 v45, v36
	v_add_u32_e32 v46, v45, v37
	v_add_u32_e32 v47, v46, v38
	v_add_u32_e32 v48, v47, v39
	v_add_u32_e32 v49, v48, v40
	v_add_u32_e32 v50, v49, v41
	v_add_u32_e32 v51, v50, v42
	v_add_u32_e32 v52, v51, v43
	v_cmp_lt_u32_e32 vcc, 0x100, v52
	v_add_u32_e32 v53, 15, v52
	v_lshrrev_b32_e32 v53, 4, v53
	v_cndmask_b32_e64 v54, 0, 1, vcc
	v_or_b32_e32 v44, v44, v54
	v_mov_b32_e32 v55, 0x26c00
	ds_max_u32 v55, v53
	ds_or_b32 v55, v44 offset:4
	s_waitcnt lgkmcnt(0)
	s_barrier
	ds_read_b64 v[0:1], v55
	v_lshlrev_b32_e32 v56, 5, v45
	v_lshlrev_b32_e32 v57, 5, v46
	v_lshlrev_b32_e32 v58, 5, v47
	v_lshlrev_b32_e32 v59, 5, v48
	v_lshlrev_b32_e32 v60, 5, v49
	v_lshlrev_b32_e32 v61, 5, v50
	v_lshlrev_b32_e32 v62, 5, v51
	v_sub_u32_e32 v56, 0x800, v56
	v_sub_u32_e32 v57, 0x1000, v57
	v_sub_u32_e32 v58, 0x1800, v58
	v_sub_u32_e32 v59, 0x2000, v59
	v_sub_u32_e32 v60, 0x2800, v60
	v_sub_u32_e32 v61, 0x3000, v61
	v_sub_u32_e32 v62, 0x3800, v62
	v_add_u32_e32 v63, s3, v75
	v_lshlrev_b32_e32 v63, 14, v63
	v_add_u32_e32 v63, 0x800000, v63
	s_waitcnt lgkmcnt(0)
	v_readfirstlane_b32 s77, v0
	v_readfirstlane_b32 s36, v1
	s_add_i32 s77, s77, 0
	s_cmp_lg_u32 s36, 0
	s_cselect_b64 s[6:7], 0, -1
	s_cmp_gt_u32 s10, 3
	s_cbranch_scc1 .Lco_done
	s_cmp_lg_u32 s36, 0
	s_cbranch_scc1 .Lco_gen
	s_mov_b32 s89, 0
.Lco_refill:
	v_mov_b32_e32 v53, 0
	v_mov_b32_e32 v0, v70
	v_cmp_lt_u32_e64 s[12:13], v0, v52
	v_cmp_le_u32_e64 s[16:17], v45, v0
	v_cmp_le_u32_e64 s[18:19], v46, v0
	v_cmp_le_u32_e64 s[20:21], v47, v0
	v_cmp_le_u32_e64 s[22:23], v48, v0
	v_cmp_le_u32_e64 s[24:25], v49, v0
	v_cmp_le_u32_e64 s[26:27], v50, v0
	v_cmp_le_u32_e64 s[28:29], v51, v0
	v_cndmask_b32_e64 v1, 0, v56, s[16:17]
	v_cndmask_b32_e64 v1, v1, v57, s[18:19]
	v_cndmask_b32_e64 v1, v1, v58, s[20:21]
	v_cndmask_b32_e64 v1, v1, v59, s[22:23]
	v_cndmask_b32_e64 v1, v1, v60, s[24:25]
	v_cndmask_b32_e64 v1, v1, v61, s[26:27]
	v_cndmask_b32_e64 v1, v1, v62, s[28:29]
	v_lshl_add_u32 v2, v0, 5, v63
	v_add_u32_e32 v2, v2, v1
	v_mov_b32_e32 v208, 0x5c3a0000
	v_mov_b32_e32 v165, 0x5c3a
	s_and_saveexec_b64 s[30:31], s[12:13]
	s_cbranch_execz .Lco_nold0
	global_load_dwordx4 v[208:211], v2, s[66:67] sc1
	global_load_dwordx2 v[164:165], v2, s[66:67] offset:16 sc1
	v_mov_b32_e32 v18, 1.0
.Lco_nold0:
	s_mov_b64 exec, s[30:31]
	v_add_u32_e32 v0, 16, v70
	v_cmp_lt_u32_e64 s[12:13], v0, v52
	v_cmp_le_u32_e64 s[16:17], v45, v0
	v_cmp_le_u32_e64 s[18:19], v46, v0
	v_cmp_le_u32_e64 s[20:21], v47, v0
	v_cmp_le_u32_e64 s[22:23], v48, v0
	v_cmp_le_u32_e64 s[24:25], v49, v0
	v_cmp_le_u32_e64 s[26:27], v50, v0
	v_cmp_le_u32_e64 s[28:29], v51, v0
	v_cndmask_b32_e64 v1, 0, v56, s[16:17]
	v_cndmask_b32_e64 v1, v1, v57, s[18:19]
	v_cndmask_b32_e64 v1, v1, v58, s[20:21]
	v_cndmask_b32_e64 v1, v1, v59, s[22:23]
	v_cndmask_b32_e64 v1, v1, v60, s[24:25]
	v_cndmask_b32_e64 v1, v1, v61, s[26:27]
	v_cndmask_b32_e64 v1, v1, v62, s[28:29]
	v_lshl_add_u32 v3, v0, 5, v63
	v_add_u32_e32 v3, v3, v1
	v_mov_b32_e32 v212, 0x5c3a0000
	v_mov_b32_e32 v167, 0x5c3a
	s_and_saveexec_b64 s[30:31], s[12:13]
	s_cbranch_execz .Lco_nold1
	global_load_dwordx4 v[212:215], v3, s[66:67] sc1
	global_load_dwordx2 v[166:167], v3, s[66:67] offset:16 sc1
	v_mov_b32_e32 v19, 1.0
.Lco_nold1:
	s_mov_b64 exec, s[30:31]
	v_add_u32_e32 v0, 32, v70
	v_cmp_lt_u32_e64 s[12:13], v0, v52
	v_cmp_le_u32_e64 s[16:17], v45, v0
	v_cmp_le_u32_e64 s[18:19], v46, v0
	v_cmp_le_u32_e64 s[20:21], v47, v0
	v_cmp_le_u32_e64 s[22:23], v48, v0
	v_cmp_le_u32_e64 s[24:25], v49, v0
	v_cmp_le_u32_e64 s[26:27], v50, v0
	v_cmp_le_u32_e64 s[28:29], v51, v0
	v_cndmask_b32_e64 v1, 0, v56, s[16:17]
	v_cndmask_b32_e64 v1, v1, v57, s[18:19]
	v_cndmask_b32_e64 v1, v1, v58, s[20:21]
	v_cndmask_b32_e64 v1, v1, v59, s[22:23]
	v_cndmask_b32_e64 v1, v1, v60, s[24:25]
	v_cndmask_b32_e64 v1, v1, v61, s[26:27]
	v_cndmask_b32_e64 v1, v1, v62, s[28:29]
	v_lshl_add_u32 v4, v0, 5, v63
	v_add_u32_e32 v4, v4, v1
	v_mov_b32_e32 v216, 0x5c3a0000
	v_mov_b32_e32 v169, 0x5c3a
	s_and_saveexec_b64 s[30:31], s[12:13]
	s_cbranch_execz .Lco_nold2
	global_load_dwordx4 v[216:219], v4, s[66:67] sc1
	global_load_dwordx2 v[168:169], v4, s[66:67] offset:16 sc1
	v_mov_b32_e32 v20, 1.0
.Lco_nold2:
	s_mov_b64 exec, s[30:31]
	v_add_u32_e32 v0, 48, v70
	v_cmp_lt_u32_e64 s[12:13], v0, v52
	v_cmp_le_u32_e64 s[16:17], v45, v0
	v_cmp_le_u32_e64 s[18:19], v46, v0
	v_cmp_le_u32_e64 s[20:21], v47, v0
	v_cmp_le_u32_e64 s[22:23], v48, v0
	v_cmp_le_u32_e64 s[24:25], v49, v0
	v_cmp_le_u32_e64 s[26:27], v50, v0
	v_cmp_le_u32_e64 s[28:29], v51, v0
	v_cndmask_b32_e64 v1, 0, v56, s[16:17]
	v_cndmask_b32_e64 v1, v1, v57, s[18:19]
	v_cndmask_b32_e64 v1, v1, v58, s[20:21]
	v_cndmask_b32_e64 v1, v1, v59, s[22:23]
	v_cndmask_b32_e64 v1, v1, v60, s[24:25]
	v_cndmask_b32_e64 v1, v1, v61, s[26:27]
	v_cndmask_b32_e64 v1, v1, v62, s[28:29]
	v_lshl_add_u32 v5, v0, 5, v63
	v_add_u32_e32 v5, v5, v1
	v_mov_b32_e32 v220, 0x5c3a0000
	v_mov_b32_e32 v171, 0x5c3a
	s_and_saveexec_b64 s[30:31], s[12:13]
	s_cbranch_execz .Lco_nold3
	global_load_dwordx4 v[220:223], v5, s[66:67] sc1
	global_load_dwordx2 v[170:171], v5, s[66:67] offset:16 sc1
	v_mov_b32_e32 v21, 1.0
.Lco_nold3:
	s_mov_b64 exec, s[30:31]
	v_add_u32_e32 v0, 64, v70
	v_cmp_lt_u32_e64 s[12:13], v0, v52
	v_cmp_le_u32_e64 s[16:17], v45, v0
	v_cmp_le_u32_e64 s[18:19], v46, v0
	v_cmp_le_u32_e64 s[20:21], v47, v0
	v_cmp_le_u32_e64 s[22:23], v48, v0
	v_cmp_le_u32_e64 s[24:25], v49, v0
	v_cmp_le_u32_e64 s[26:27], v50, v0
	v_cmp_le_u32_e64 s[28:29], v51, v0
	v_cndmask_b32_e64 v1, 0, v56, s[16:17]
	v_cndmask_b32_e64 v1, v1, v57, s[18:19]
	v_cndmask_b32_e64 v1, v1, v58, s[20:21]
	v_cndmask_b32_e64 v1, v1, v59, s[22:23]
	v_cndmask_b32_e64 v1, v1, v60, s[24:25]
	v_cndmask_b32_e64 v1, v1, v61, s[26:27]
	v_cndmask_b32_e64 v1, v1, v62, s[28:29]
	v_lshl_add_u32 v6, v0, 5, v63
	v_add_u32_e32 v6, v6, v1
	v_mov_b32_e32 v224, 0x5c3a0000
	v_mov_b32_e32 v173, 0x5c3a
	s_and_saveexec_b64 s[30:31], s[12:13]
	s_cbranch_execz .Lco_nold4
	global_load_dwordx4 v[224:227], v6, s[66:67] sc1
	global_load_dwordx2 v[172:173], v6, s[66:67] offset:16 sc1
	v_mov_b32_e32 v22, 1.0
.Lco_nold4:
	s_mov_b64 exec, s[30:31]
	v_add_u32_e32 v0, 80, v70
	v_cmp_lt_u32_e64 s[12:13], v0, v52
	v_cmp_le_u32_e64 s[16:17], v45, v0
	v_cmp_le_u32_e64 s[18:19], v46, v0
	v_cmp_le_u32_e64 s[20:21], v47, v0
	v_cmp_le_u32_e64 s[22:23], v48, v0
	v_cmp_le_u32_e64 s[24:25], v49, v0
	v_cmp_le_u32_e64 s[26:27], v50, v0
	v_cmp_le_u32_e64 s[28:29], v51, v0
	v_cndmask_b32_e64 v1, 0, v56, s[16:17]
	v_cndmask_b32_e64 v1, v1, v57, s[18:19]
	v_cndmask_b32_e64 v1, v1, v58, s[20:21]
	v_cndmask_b32_e64 v1, v1, v59, s[22:23]
	v_cndmask_b32_e64 v1, v1, v60, s[24:25]
	v_cndmask_b32_e64 v1, v1, v61, s[26:27]
	v_cndmask_b32_e64 v1, v1, v62, s[28:29]
	v_lshl_add_u32 v7, v0, 5, v63
	v_add_u32_e32 v7, v7, v1
	v_mov_b32_e32 v228, 0x5c3a0000
	v_mov_b32_e32 v175, 0x5c3a
	s_and_saveexec_b64 s[30:31], s[12:13]
	s_cbranch_execz .Lco_nold5
	global_load_dwordx4 v[228:231], v7, s[66:67] sc1
	global_load_dwordx2 v[174:175], v7, s[66:67] offset:16 sc1
	v_mov_b32_e32 v23, 1.0
.Lco_nold5:
	s_mov_b64 exec, s[30:31]
	v_add_u32_e32 v0, 96, v70
	v_cmp_lt_u32_e64 s[12:13], v0, v52
	v_cmp_le_u32_e64 s[16:17], v45, v0
	v_cmp_le_u32_e64 s[18:19], v46, v0
	v_cmp_le_u32_e64 s[20:21], v47, v0
	v_cmp_le_u32_e64 s[22:23], v48, v0
	v_cmp_le_u32_e64 s[24:25], v49, v0
	v_cmp_le_u32_e64 s[26:27], v50, v0
	v_cmp_le_u32_e64 s[28:29], v51, v0
	v_cndmask_b32_e64 v1, 0, v56, s[16:17]
	v_cndmask_b32_e64 v1, v1, v57, s[18:19]
	v_cndmask_b32_e64 v1, v1, v58, s[20:21]
	v_cndmask_b32_e64 v1, v1, v59, s[22:23]
	v_cndmask_b32_e64 v1, v1, v60, s[24:25]
	v_cndmask_b32_e64 v1, v1, v61, s[26:27]
	v_cndmask_b32_e64 v1, v1, v62, s[28:29]
	v_lshl_add_u32 v10, v0, 5, v63
	v_add_u32_e32 v10, v10, v1
	v_mov_b32_e32 v232, 0x5c3a0000
	v_mov_b32_e32 v177, 0x5c3a
	s_and_saveexec_b64 s[30:31], s[12:13]
	s_cbranch_execz .Lco_nold6
	global_load_dwordx4 v[232:235], v10, s[66:67] sc1
	global_load_dwordx2 v[176:177], v10, s[66:67] offset:16 sc1
	v_mov_b32_e32 v24, 1.0
.Lco_nold6:
	s_mov_b64 exec, s[30:31]
	v_add_u32_e32 v0, 112, v70
	v_cmp_lt_u32_e64 s[12:13], v0, v52
	v_cmp_le_u32_e64 s[16:17], v45, v0
	v_cmp_le_u32_e64 s[18:19], v46, v0
	v_cmp_le_u32_e64 s[20:21], v47, v0
	v_cmp_le_u32_e64 s[22:23], v48, v0
	v_cmp_le_u32_e64 s[24:25], v49, v0
	v_cmp_le_u32_e64 s[26:27], v50, v0
	v_cmp_le_u32_e64 s[28:29], v51, v0
	v_cndmask_b32_e64 v1, 0, v56, s[16:17]
	v_cndmask_b32_e64 v1, v1, v57, s[18:19]
	v_cndmask_b32_e64 v1, v1, v58, s[20:21]
	v_cndmask_b32_e64 v1, v1, v59, s[22:23]
	v_cndmask_b32_e64 v1, v1, v60, s[24:25]
	v_cndmask_b32_e64 v1, v1, v61, s[26:27]
	v_cndmask_b32_e64 v1, v1, v62, s[28:29]
	v_lshl_add_u32 v11, v0, 5, v63
	v_add_u32_e32 v11, v11, v1
	v_mov_b32_e32 v236, 0x5c3a0000
	v_mov_b32_e32 v179, 0x5c3a
	s_and_saveexec_b64 s[30:31], s[12:13]
	s_cbranch_execz .Lco_nold7
	global_load_dwordx4 v[236:239], v11, s[66:67] sc1
	global_load_dwordx2 v[178:179], v11, s[66:67] offset:16 sc1
	v_mov_b32_e32 v25, 1.0
.Lco_nold7:
	s_mov_b64 exec, s[30:31]
	s_cmp_gt_i32 s77, 8
	s_cbranch_scc0 .Lco_ld_done
	v_add_u32_e32 v0, 128, v70
	v_cmp_lt_u32_e64 s[12:13], v0, v52
	v_cmp_le_u32_e64 s[16:17], v45, v0
	v_cmp_le_u32_e64 s[18:19], v46, v0
	v_cmp_le_u32_e64 s[20:21], v47, v0
	v_cmp_le_u32_e64 s[22:23], v48, v0
	v_cmp_le_u32_e64 s[24:25], v49, v0
	v_cmp_le_u32_e64 s[26:27], v50, v0
	v_cmp_le_u32_e64 s[28:29], v51, v0
	v_cndmask_b32_e64 v1, 0, v56, s[16:17]
	v_cndmask_b32_e64 v1, v1, v57, s[18:19]
	v_cndmask_b32_e64 v1, v1, v58, s[20:21]
	v_cndmask_b32_e64 v1, v1, v59, s[22:23]
	v_cndmask_b32_e64 v1, v1, v60, s[24:25]
	v_cndmask_b32_e64 v1, v1, v61, s[26:27]
	v_cndmask_b32_e64 v1, v1, v62, s[28:29]
	v_lshl_add_u32 v12, v0, 5, v63
	v_add_u32_e32 v12, v12, v1
	v_mov_b32_e32 v240, 0x5c3a0000
	v_mov_b32_e32 v181, 0x5c3a
	s_and_saveexec_b64 s[30:31], s[12:13]
	s_cbranch_execz .Lco_nold8
	global_load_dwordx4 v[240:243], v12, s[66:67] sc1
	global_load_dwordx2 v[180:181], v12, s[66:67] offset:16 sc1
	v_mov_b32_e32 v26, 1.0
.Lco_nold8:
	s_mov_b64 exec, s[30:31]
	v_add_u32_e32 v0, 144, v70
	v_cmp_lt_u32_e64 s[12:13], v0, v52
	v_cmp_le_u32_e64 s[16:17], v45, v0
	v_cmp_le_u32_e64 s[18:19], v46, v0
	v_cmp_le_u32_e64 s[20:21], v47, v0
	v_cmp_le_u32_e64 s[22:23], v48, v0
	v_cmp_le_u32_e64 s[24:25], v49, v0
	v_cmp_le_u32_e64 s[26:27], v50, v0
	v_cmp_le_u32_e64 s[28:29], v51, v0
	v_cndmask_b32_e64 v1, 0, v56, s[16:17]
	v_cndmask_b32_e64 v1, v1, v57, s[18:19]
	v_cndmask_b32_e64 v1, v1, v58, s[20:21]
	v_cndmask_b32_e64 v1, v1, v59, s[22:23]
	v_cndmask_b32_e64 v1, v1, v60, s[24:25]
	v_cndmask_b32_e64 v1, v1, v61, s[26:27]
	v_cndmask_b32_e64 v1, v1, v62, s[28:29]
	v_lshl_add_u32 v13, v0, 5, v63
	v_add_u32_e32 v13, v13, v1
	v_mov_b32_e32 v244, 0x5c3a0000
	v_mov_b32_e32 v183, 0x5c3a
	s_and_saveexec_b64 s[30:31], s[12:13]
	s_cbranch_execz .Lco_nold9
	global_load_dwordx4 v[244:247], v13, s[66:67] sc1
	global_load_dwordx2 v[182:183], v13, s[66:67] offset:16 sc1
	v_mov_b32_e32 v27, 1.0
.Lco_nold9:
	s_mov_b64 exec, s[30:31]
	s_cmp_gt_i32 s77, 10
	s_cbranch_scc0 .Lco_ld_done
	v_add_u32_e32 v0, 160, v70
	v_cmp_lt_u32_e64 s[12:13], v0, v52
	v_cmp_le_u32_e64 s[16:17], v45, v0
	v_cmp_le_u32_e64 s[18:19], v46, v0
	v_cmp_le_u32_e64 s[20:21], v47, v0
	v_cmp_le_u32_e64 s[22:23], v48, v0
	v_cmp_le_u32_e64 s[24:25], v49, v0
	v_cmp_le_u32_e64 s[26:27], v50, v0
	v_cmp_le_u32_e64 s[28:29], v51, v0
	v_cndmask_b32_e64 v1, 0, v56, s[16:17]
	v_cndmask_b32_e64 v1, v1, v57, s[18:19]
	v_cndmask_b32_e64 v1, v1, v58, s[20:21]
	v_cndmask_b32_e64 v1, v1, v59, s[22:23]
	v_cndmask_b32_e64 v1, v1, v60, s[24:25]
	v_cndmask_b32_e64 v1, v1, v61, s[26:27]
	v_cndmask_b32_e64 v1, v1, v62, s[28:29]
	v_lshl_add_u32 v14, v0, 5, v63
	v_add_u32_e32 v14, v14, v1
	v_mov_b32_e32 v248, 0x5c3a0000
	v_mov_b32_e32 v185, 0x5c3a
	s_and_saveexec_b64 s[30:31], s[12:13]
	s_cbranch_execz .Lco_nold10
	global_load_dwordx4 v[248:251], v14, s[66:67] sc1
	global_load_dwordx2 v[184:185], v14, s[66:67] offset:16 sc1
	v_mov_b32_e32 v28, 1.0
.Lco_nold10:
	s_mov_b64 exec, s[30:31]
	v_add_u32_e32 v0, 176, v70
	v_cmp_lt_u32_e64 s[12:13], v0, v52
	v_cmp_le_u32_e64 s[16:17], v45, v0
	v_cmp_le_u32_e64 s[18:19], v46, v0
	v_cmp_le_u32_e64 s[20:21], v47, v0
	v_cmp_le_u32_e64 s[22:23], v48, v0
	v_cmp_le_u32_e64 s[24:25], v49, v0
	v_cmp_le_u32_e64 s[26:27], v50, v0
	v_cmp_le_u32_e64 s[28:29], v51, v0
	v_cndmask_b32_e64 v1, 0, v56, s[16:17]
	v_cndmask_b32_e64 v1, v1, v57, s[18:19]
	v_cndmask_b32_e64 v1, v1, v58, s[20:21]
	v_cndmask_b32_e64 v1, v1, v59, s[22:23]
	v_cndmask_b32_e64 v1, v1, v60, s[24:25]
	v_cndmask_b32_e64 v1, v1, v61, s[26:27]
	v_cndmask_b32_e64 v1, v1, v62, s[28:29]
	v_lshl_add_u32 v15, v0, 5, v63
	v_add_u32_e32 v15, v15, v1
	v_mov_b32_e32 v186, 0x5c3a0000
	v_mov_b32_e32 v37, 0x5c3a
	s_and_saveexec_b64 s[30:31], s[12:13]
	s_cbranch_execz .Lco_nold11
	global_load_dwordx4 v[186:189], v15, s[66:67] sc1
	global_load_dwordx2 v[36:37], v15, s[66:67] offset:16 sc1
	v_mov_b32_e32 v29, 1.0
.Lco_nold11:
	s_mov_b64 exec, s[30:31]
	v_add_u32_e32 v0, 192, v70
	v_cmp_lt_u32_e64 s[12:13], v0, v52
	v_cmp_le_u32_e64 s[16:17], v45, v0
	v_cmp_le_u32_e64 s[18:19], v46, v0
	v_cmp_le_u32_e64 s[20:21], v47, v0
	v_cmp_le_u32_e64 s[22:23], v48, v0
	v_cmp_le_u32_e64 s[24:25], v49, v0
	v_cmp_le_u32_e64 s[26:27], v50, v0
	v_cmp_le_u32_e64 s[28:29], v51, v0
	v_cndmask_b32_e64 v1, 0, v56, s[16:17]
	v_cndmask_b32_e64 v1, v1, v57, s[18:19]
	v_cndmask_b32_e64 v1, v1, v58, s[20:21]
	v_cndmask_b32_e64 v1, v1, v59, s[22:23]
	v_cndmask_b32_e64 v1, v1, v60, s[24:25]
	v_cndmask_b32_e64 v1, v1, v61, s[26:27]
	v_cndmask_b32_e64 v1, v1, v62, s[28:29]
	v_lshl_add_u32 v35, v0, 5, v63
	v_add_u32_e32 v35, v35, v1
	v_mov_b32_e32 v190, 0x5c3a0000
	v_mov_b32_e32 v39, 0x5c3a
	s_and_saveexec_b64 s[30:31], s[12:13]
	s_cbranch_execz .Lco_nold12
	global_load_dwordx4 v[190:193], v35, s[66:67] sc1
	global_load_dwordx2 v[38:39], v35, s[66:67] offset:16 sc1
	v_mov_b32_e32 v30, 1.0
.Lco_nold12:
	s_mov_b64 exec, s[30:31]
	v_add_u32_e32 v0, 208, v70
	v_cmp_lt_u32_e64 s[12:13], v0, v52
	v_cmp_le_u32_e64 s[16:17], v45, v0
	v_cmp_le_u32_e64 s[18:19], v46, v0
	v_cmp_le_u32_e64 s[20:21], v47, v0
	v_cmp_le_u32_e64 s[22:23], v48, v0
	v_cmp_le_u32_e64 s[24:25], v49, v0
	v_cmp_le_u32_e64 s[26:27], v50, v0
	v_cmp_le_u32_e64 s[28:29], v51, v0
	v_cndmask_b32_e64 v1, 0, v56, s[16:17]
	v_cndmask_b32_e64 v1, v1, v57, s[18:19]
	v_cndmask_b32_e64 v1, v1, v58, s[20:21]
	v_cndmask_b32_e64 v1, v1, v59, s[22:23]
	v_cndmask_b32_e64 v1, v1, v60, s[24:25]
	v_cndmask_b32_e64 v1, v1, v61, s[26:27]
	v_cndmask_b32_e64 v1, v1, v62, s[28:29]
	v_lshl_add_u32 v64, v0, 5, v63
	v_add_u32_e32 v64, v64, v1
	v_mov_b32_e32 v194, 0x5c3a0000
	v_mov_b32_e32 v41, 0x5c3a
	s_and_saveexec_b64 s[30:31], s[12:13]
	s_cbranch_execz .Lco_nold13
	global_load_dwordx4 v[194:197], v64, s[66:67] sc1
	global_load_dwordx2 v[40:41], v64, s[66:67] offset:16 sc1
	v_mov_b32_e32 v31, 1.0
.Lco_nold13:
	s_mov_b64 exec, s[30:31]
	v_add_u32_e32 v0, 224, v70
	v_cmp_lt_u32_e64 s[12:13], v0, v52
	v_cmp_le_u32_e64 s[16:17], v45, v0
	v_cmp_le_u32_e64 s[18:19], v46, v0
	v_cmp_le_u32_e64 s[20:21], v47, v0
	v_cmp_le_u32_e64 s[22:23], v48, v0
	v_cmp_le_u32_e64 s[24:25], v49, v0
	v_cmp_le_u32_e64 s[26:27], v50, v0
	v_cmp_le_u32_e64 s[28:29], v51, v0
	v_cndmask_b32_e64 v1, 0, v56, s[16:17]
	v_cndmask_b32_e64 v1, v1, v57, s[18:19]
	v_cndmask_b32_e64 v1, v1, v58, s[20:21]
	v_cndmask_b32_e64 v1, v1, v59, s[22:23]
	v_cndmask_b32_e64 v1, v1, v60, s[24:25]
	v_cndmask_b32_e64 v1, v1, v61, s[26:27]
	v_cndmask_b32_e64 v1, v1, v62, s[28:29]
	v_lshl_add_u32 v65, v0, 5, v63
	v_add_u32_e32 v65, v65, v1
	v_mov_b32_e32 v198, 0x5c3a0000
	v_mov_b32_e32 v43, 0x5c3a
	s_and_saveexec_b64 s[30:31], s[12:13]
	s_cbranch_execz .Lco_nold14
	global_load_dwordx4 v[198:201], v65, s[66:67] sc1
	global_load_dwordx2 v[42:43], v65, s[66:67] offset:16 sc1
	v_mov_b32_e32 v32, 1.0
.Lco_nold14:
	s_mov_b64 exec, s[30:31]
	v_add_u32_e32 v0, 240, v70
	v_cmp_lt_u32_e64 s[12:13], v0, v52
	v_cmp_le_u32_e64 s[16:17], v45, v0
	v_cmp_le_u32_e64 s[18:19], v46, v0
	v_cmp_le_u32_e64 s[20:21], v47, v0
	v_cmp_le_u32_e64 s[22:23], v48, v0
	v_cmp_le_u32_e64 s[24:25], v49, v0
	v_cmp_le_u32_e64 s[26:27], v50, v0
	v_cmp_le_u32_e64 s[28:29], v51, v0
	v_cndmask_b32_e64 v1, 0, v56, s[16:17]
	v_cndmask_b32_e64 v1, v1, v57, s[18:19]
	v_cndmask_b32_e64 v1, v1, v58, s[20:21]
	v_cndmask_b32_e64 v1, v1, v59, s[22:23]
	v_cndmask_b32_e64 v1, v1, v60, s[24:25]
	v_cndmask_b32_e64 v1, v1, v61, s[26:27]
	v_cndmask_b32_e64 v1, v1, v62, s[28:29]
	v_lshl_add_u32 v66, v0, 5, v63
	v_add_u32_e32 v66, v66, v1
	v_mov_b32_e32 v202, 0x5c3a0000
	v_mov_b32_e32 v55, 0x5c3a
	s_and_saveexec_b64 s[30:31], s[12:13]
	s_cbranch_execz .Lco_nold15
	global_load_dwordx4 v[202:205], v66, s[66:67] sc1
	global_load_dwordx2 v[54:55], v66, s[66:67] offset:16 sc1
	v_mov_b32_e32 v33, 1.0

.Lco_ld_done:
	s_waitcnt vmcnt(0)
	v_lshrrev_b32_e32 v1, 16, v208
	v_xor_b32_e32 v1, 0x5c3a, v1
	v_xor_b32_e32 v0, 0x5c3a, v165
	v_or3_b32 v53, v53, v1, v0
	v_lshrrev_b32_e32 v1, 16, v212
	v_xor_b32_e32 v1, 0x5c3a, v1
	v_xor_b32_e32 v0, 0x5c3a, v167
	v_or3_b32 v53, v53, v1, v0
	v_lshrrev_b32_e32 v1, 16, v216
	v_xor_b32_e32 v1, 0x5c3a, v1
	v_xor_b32_e32 v0, 0x5c3a, v169
	v_or3_b32 v53, v53, v1, v0
	v_lshrrev_b32_e32 v1, 16, v220
	v_xor_b32_e32 v1, 0x5c3a, v1
	v_xor_b32_e32 v0, 0x5c3a, v171
	v_or3_b32 v53, v53, v1, v0
	v_lshrrev_b32_e32 v1, 16, v224
	v_xor_b32_e32 v1, 0x5c3a, v1
	v_xor_b32_e32 v0, 0x5c3a, v173
	v_or3_b32 v53, v53, v1, v0
	v_lshrrev_b32_e32 v1, 16, v228
	v_xor_b32_e32 v1, 0x5c3a, v1
	v_xor_b32_e32 v0, 0x5c3a, v175
	v_or3_b32 v53, v53, v1, v0
	v_lshrrev_b32_e32 v1, 16, v232
	v_xor_b32_e32 v1, 0x5c3a, v1
	v_xor_b32_e32 v0, 0x5c3a, v177
	v_or3_b32 v53, v53, v1, v0
	v_lshrrev_b32_e32 v1, 16, v236
	v_xor_b32_e32 v1, 0x5c3a, v1
	v_xor_b32_e32 v0, 0x5c3a, v179
	v_or3_b32 v53, v53, v1, v0
	s_cmp_gt_i32 s77, 8
	s_cbranch_scc0 .Lco_chk_done
	v_lshrrev_b32_e32 v1, 16, v240
	v_xor_b32_e32 v1, 0x5c3a, v1
	v_xor_b32_e32 v0, 0x5c3a, v181
	v_or3_b32 v53, v53, v1, v0
	v_lshrrev_b32_e32 v1, 16, v244
	v_xor_b32_e32 v1, 0x5c3a, v1
	v_xor_b32_e32 v0, 0x5c3a, v183
	v_or3_b32 v53, v53, v1, v0
	s_cmp_gt_i32 s77, 10
	s_cbranch_scc0 .Lco_chk_done
	v_lshrrev_b32_e32 v1, 16, v248
	v_xor_b32_e32 v1, 0x5c3a, v1
	v_xor_b32_e32 v0, 0x5c3a, v185
	v_or3_b32 v53, v53, v1, v0
	v_lshrrev_b32_e32 v1, 16, v186
	v_xor_b32_e32 v1, 0x5c3a, v1
	v_xor_b32_e32 v0, 0x5c3a, v37
	v_or3_b32 v53, v53, v1, v0
	v_lshrrev_b32_e32 v1, 16, v190
	v_xor_b32_e32 v1, 0x5c3a, v1
	v_xor_b32_e32 v0, 0x5c3a, v39
	v_or3_b32 v53, v53, v1, v0
	v_lshrrev_b32_e32 v1, 16, v194
	v_xor_b32_e32 v1, 0x5c3a, v1
	v_xor_b32_e32 v0, 0x5c3a, v41
	v_or3_b32 v53, v53, v1, v0
	v_lshrrev_b32_e32 v1, 16, v198
	v_xor_b32_e32 v1, 0x5c3a, v1
	v_xor_b32_e32 v0, 0x5c3a, v43
	v_or3_b32 v53, v53, v1, v0
	v_lshrrev_b32_e32 v1, 16, v202
	v_xor_b32_e32 v1, 0x5c3a, v1
	v_xor_b32_e32 v0, 0x5c3a, v55
	v_or3_b32 v53, v53, v1, v0
.Lco_chk_done:
	v_cmp_ne_u32_e32 vcc, 0, v53
	s_add_i32 s89, s89, 1
	s_nop 0
	s_cbranch_vccz .Lco_chk_ok
	s_cmp_lt_u32 s89, 0x4000
	s_cbranch_scc1 .Lco_refill
.Lco_chk_ok:
	v_cmp_lt_u32_e64 s[12:13], v70, v52
	v_mov_b32_e32 v159, 0xf000
	s_nop 0
	s_and_saveexec_b64 s[30:31], s[12:13]
	v_and_b32_e32 v159, 0xffff, v208
	v_mov_b32_e32 v71, v164
	v_mov_b32_e32 v9, v209
	v_mov_b32_e32 v129, v210
	v_mov_b32_e32 v130, v211
	s_mov_b64 exec, s[30:31]
	v_add_u32_e32 v0, 16, v70
	v_cmp_lt_u32_e64 s[12:13], v0, v52
	v_mov_b32_e32 v158, 0xf000
	s_nop 0
	s_and_saveexec_b64 s[30:31], s[12:13]
	v_and_b32_e32 v158, 0xffff, v212
	v_mov_b32_e32 v81, v166
	v_mov_b32_e32 v131, v213
	v_mov_b32_e32 v132, v214
	v_mov_b32_e32 v133, v215
	s_mov_b64 exec, s[30:31]
	v_add_u32_e32 v0, 32, v70
	v_cmp_lt_u32_e64 s[12:13], v0, v52
	v_mov_b32_e32 v157, 0xf000
	s_nop 0
	s_and_saveexec_b64 s[30:31], s[12:13]
	v_and_b32_e32 v157, 0xffff, v216
	v_mov_b32_e32 v85, v168
	v_mov_b32_e32 v134, v217
	v_mov_b32_e32 v135, v218
	v_mov_b32_e32 v136, v219
	s_mov_b64 exec, s[30:31]
	v_add_u32_e32 v0, 48, v70
	v_cmp_lt_u32_e64 s[12:13], v0, v52
	v_mov_b32_e32 v156, 0xf000
	s_nop 0
	s_and_saveexec_b64 s[30:31], s[12:13]
	v_and_b32_e32 v156, 0xffff, v220
	v_mov_b32_e32 v86, v170
	v_mov_b32_e32 v137, v221
	v_mov_b32_e32 v138, v222
	v_mov_b32_e32 v139, v223
	s_mov_b64 exec, s[30:31]
	v_add_u32_e32 v0, 64, v70
	v_cmp_lt_u32_e64 s[12:13], v0, v52
	v_mov_b32_e32 v155, 0xf000
	s_nop 0
	s_and_saveexec_b64 s[30:31], s[12:13]
	v_and_b32_e32 v155, 0xffff, v224
	v_mov_b32_e32 v87, v172
	v_mov_b32_e32 v140, v225
	v_mov_b32_e32 v141, v226
	v_mov_b32_e32 v142, v227
	s_mov_b64 exec, s[30:31]
	v_add_u32_e32 v0, 80, v70
	v_cmp_lt_u32_e64 s[12:13], v0, v52
	v_mov_b32_e32 v154, 0xf000
	s_nop 0
	s_and_saveexec_b64 s[30:31], s[12:13]
	v_and_b32_e32 v154, 0xffff, v228
	v_mov_b32_e32 v88, v174
	v_mov_b32_e32 v143, v229
	v_mov_b32_e32 v144, v230
	v_mov_b32_e32 v145, v231
	s_mov_b64 exec, s[30:31]
	v_add_u32_e32 v0, 96, v70
	v_cmp_lt_u32_e64 s[12:13], v0, v52
	v_mov_b32_e32 v153, 0xf000
	s_nop 0
	s_and_saveexec_b64 s[30:31], s[12:13]
	v_and_b32_e32 v153, 0xffff, v232
	v_mov_b32_e32 v89, v176
	v_mov_b32_e32 v146, v233
	v_mov_b32_e32 v147, v234
	v_mov_b32_e32 v148, v235
	s_mov_b64 exec, s[30:31]
	v_add_u32_e32 v0, 112, v70
	v_cmp_lt_u32_e64 s[12:13], v0, v52
	v_mov_b32_e32 v149, 0xf000
	s_nop 0
	s_and_saveexec_b64 s[30:31], s[12:13]
	v_and_b32_e32 v149, 0xffff, v236
	v_mov_b32_e32 v90, v178
	v_mov_b32_e32 v150, v237
	v_mov_b32_e32 v151, v238
	v_mov_b32_e32 v152, v239
	s_mov_b64 exec, s[30:31]
	s_cmp_gt_i32 s77, 8
	s_cbranch_scc0 .Lco_done
	v_add_u32_e32 v0, 128, v70
	v_cmp_lt_u32_e64 s[12:13], v0, v52
	v_mov_b32_e32 v128, 0xf000
	s_nop 0
	s_and_saveexec_b64 s[30:31], s[12:13]
	v_and_b32_e32 v128, 0xffff, v240
	v_mov_b32_e32 v91, v180
	v_mov_b32_e32 v121, v241
	v_mov_b32_e32 v123, v242
	v_mov_b32_e32 v125, v243
	s_mov_b64 exec, s[30:31]
	v_add_u32_e32 v0, 144, v70
	v_cmp_lt_u32_e64 s[12:13], v0, v52
	v_mov_b32_e32 v127, 0xf000
	s_nop 0
	s_and_saveexec_b64 s[30:31], s[12:13]
	v_and_b32_e32 v127, 0xffff, v244
	v_mov_b32_e32 v92, v182
	v_mov_b32_e32 v122, v245
	v_mov_b32_e32 v124, v246
	v_mov_b32_e32 v126, v247
	s_mov_b64 exec, s[30:31]
	s_cmp_gt_i32 s77, 10
	s_cbranch_scc0 .Lco_done
	v_add_u32_e32 v0, 160, v70
	v_cmp_lt_u32_e64 s[12:13], v0, v52
	v_mov_b32_e32 v120, 0xf000
	s_nop 0
	s_and_saveexec_b64 s[30:31], s[12:13]
	v_and_b32_e32 v120, 0xffff, v248
	v_mov_b32_e32 v93, v184
	v_mov_b32_e32 v112, v249
	v_mov_b32_e32 v115, v250
	v_mov_b32_e32 v117, v251
	s_mov_b64 exec, s[30:31]
	v_add_u32_e32 v0, 176, v70
	v_cmp_lt_u32_e64 s[12:13], v0, v52
	v_mov_b32_e32 v119, 0xf000
	s_nop 0
	s_and_saveexec_b64 s[30:31], s[12:13]
	v_and_b32_e32 v119, 0xffff, v186
	v_mov_b32_e32 v94, v36
	v_mov_b32_e32 v113, v187
	v_mov_b32_e32 v116, v188
	v_mov_b32_e32 v118, v189
	s_mov_b64 exec, s[30:31]
	v_add_u32_e32 v0, 192, v70
	v_cmp_lt_u32_e64 s[12:13], v0, v52
	v_mov_b32_e32 v114, 0xf000
	s_nop 0
	s_and_saveexec_b64 s[30:31], s[12:13]
	v_and_b32_e32 v114, 0xffff, v190
	v_mov_b32_e32 v95, v38
	v_mov_b32_e32 v100, v191
	v_mov_b32_e32 v103, v192
	v_mov_b32_e32 v107, v193
	s_mov_b64 exec, s[30:31]
	v_add_u32_e32 v0, 208, v70
	v_cmp_lt_u32_e64 s[12:13], v0, v52
	v_mov_b32_e32 v111, 0xf000
	s_nop 0
	s_and_saveexec_b64 s[30:31], s[12:13]
	v_and_b32_e32 v111, 0xffff, v194
	v_mov_b32_e32 v96, v40
	v_mov_b32_e32 v101, v195
	v_mov_b32_e32 v104, v196
	v_mov_b32_e32 v108, v197
	s_mov_b64 exec, s[30:31]
	v_add_u32_e32 v0, 224, v70
	v_cmp_lt_u32_e64 s[12:13], v0, v52
	v_mov_b32_e32 v17, 0xf000
	s_nop 0
	s_and_saveexec_b64 s[30:31], s[12:13]
	v_and_b32_e32 v17, 0xffff, v198
	v_mov_b32_e32 v97, v42
	v_mov_b32_e32 v102, v199
	v_mov_b32_e32 v105, v200
	v_mov_b32_e32 v109, v201
	s_mov_b64 exec, s[30:31]
	v_add_u32_e32 v0, 240, v70
	v_cmp_lt_u32_e64 s[12:13], v0, v52
	v_mov_b32_e32 v8, 0xf000
	s_nop 0
	s_and_saveexec_b64 s[30:31], s[12:13]
	v_and_b32_e32 v8, 0xffff, v202
	v_mov_b32_e32 v99, v54
	v_mov_b32_e32 v16, v203
	v_mov_b32_e32 v106, v204
	v_mov_b32_e32 v110, v205
	s_mov_b64 exec, s[30:31]
	s_branch .Lco_done
